# grid barrier: acquire-side cache invalidate issued at arrival (overlaps the arrival atomic and the wait), late invalidates dropped
# speedup vs baseline: 1.0198x; 1.0032x over previous
; __device__ __forceinline__ unsigned xb_add(unsigned* p, unsigned v) { return __hip_atomic_fetch_add(p, v, __ATOMIC_RELAXED, __HIP_MEMORY_SCOPE_AGENT); }
; __device__ __forceinline__ void xcd_barrier(const XcdBarrier& b) {
;     ...
;             __builtin_amdgcn_fence(__ATOMIC_ACQUIRE, "agent");
;             xb_add(&bar[XB_XGEN(b.x)], 1u);
;             asm volatile("s_waitcnt vmcnt(0)" ::: "memory");
.LBB0_190:
	s_or_b64 exec, exec, s[0:1]
	v_readlane_b32 s0, v247, 57
	v_readlane_b32 s1, v247, 58
	s_waitcnt vmcnt(0)
	s_nop 2
	s_waitcnt vmcnt(0)

; __device__ __forceinline__ unsigned xb_ld(unsigned* p)              { return __hip_atomic_load(p, __ATOMIC_RELAXED, __HIP_MEMORY_SCOPE_AGENT); }
; __device__ __forceinline__ unsigned xb_add(unsigned* p, unsigned v) { return __hip_atomic_fetch_add(p, v, __ATOMIC_RELAXED, __HIP_MEMORY_SCOPE_AGENT); }
; #define XB_SPIN(cond, bar) do { unsigned _sp = 0; while (cond) { __builtin_amdgcn_s_sleep(1); \
;     if ((++_sp & 255u) == 0u) { if (xb_ld(&(bar)[XB_TMO])) break; if (_sp > XB_SPIN_CAP) { atomicAdd(&(bar)[XB_TMO], 1u); break; } } } } while (0)
; __device__ __forceinline__ void xcd_barrier(const XcdBarrier& b) {
;     ...
;         const unsigned old = xb_add(&bar[XB_XSUB(b.x)], 1u);
;         const unsigned gen = old / nloc;
;         if (old + 1u == (gen + 1u) * nloc) {
;             __builtin_amdgcn_fence(__ATOMIC_RELEASE, "agent");
;             asm volatile("s_waitcnt vmcnt(0)" ::: "memory");
;             const unsigned og = xb_add(&bar[XB_TOP], 1u);
;             const unsigned tg = og / nx;
;             if (og + 1u == (tg + 1u) * nx) xb_add(&bar[XB_TOPGEN], 1u);
;             else XB_SPIN(xb_ld(&bar[XB_TOPGEN]) == tg, bar);
;             __builtin_amdgcn_fence(__ATOMIC_ACQUIRE, "agent");
;             xb_add(&bar[XB_XGEN(b.x)], 1u);
;             asm volatile("s_waitcnt vmcnt(0)" ::: "memory");
;         } else {
;             XB_SPIN(xb_ld(&bar[XB_XGEN(b.x)]) == gen, bar);
.LBB0_229:
	v_readlane_b32 s0, v247, 55
	v_readlane_b32 s1, v247, 56
	v_cvt_f32_u32_e32 v1, v2
	v_sub_u32_e32 v4, 0, v2
	v_rcp_iflag_f32_e32 v1, v1
	s_nop 1
	buffer_inv sc1
	global_atomic_add v3, v153, v197, s[0:1] sc0
	v_mul_f32_e32 v1, 0x4f7ffffe, v1
	v_cvt_u32_f32_e32 v1, v1
	v_mul_lo_u32 v4, v4, v1
	v_mul_hi_u32 v4, v1, v4
	v_add_u32_e32 v1, v1, v4
	s_waitcnt vmcnt(0)
	v_mul_hi_u32 v1, v3, v1
	v_mul_lo_u32 v4, v1, v2
	v_sub_u32_e32 v4, v3, v4
	v_add_u32_e32 v5, 1, v1
	v_cmp_ge_u32_e32 vcc, v4, v2
	v_add_u32_e32 v3, 1, v3
	s_nop 0
	v_cndmask_b32_e32 v1, v1, v5, vcc
	v_sub_u32_e32 v5, v4, v2
	v_cndmask_b32_e32 v4, v4, v5, vcc
	v_add_u32_e32 v5, 1, v1
	v_cmp_ge_u32_e32 vcc, v4, v2
	s_nop 1
	v_cndmask_b32_e32 v1, v1, v5, vcc
	v_mul_lo_u32 v4, v2, v1
	v_add_u32_e32 v2, v4, v2
	v_cmp_ne_u32_e32 vcc, v3, v2
	s_and_saveexec_b64 s[0:1], vcc
	s_xor_b64 s[0:1], exec, s[0:1]
	s_cbranch_execz .LBB0_243
	v_readlane_b32 s2, v247, 61
	v_readlane_b32 s3, v247, 62
	s_waitcnt lgkmcnt(0)
	s_nop 3
	global_load_dword v0, v153, s[2:3] sc1
	s_waitcnt vmcnt(0)
	v_cmp_eq_u32_e32 vcc, v0, v1
	s_and_saveexec_b64 s[10:11], vcc
	s_cbranch_execz .LBB0_242
	s_mov_b32 s31, 1
	s_mov_b64 s[12:13], 0
	s_branch .LBB0_233

; __device__ __forceinline__ unsigned xb_ld(unsigned* p)              { return __hip_atomic_load(p, __ATOMIC_RELAXED, __HIP_MEMORY_SCOPE_AGENT); }
; #define XB_SPIN(cond, bar) do { unsigned _sp = 0; while (cond) { __builtin_amdgcn_s_sleep(1); \
;     if ((++_sp & 255u) == 0u) { if (xb_ld(&(bar)[XB_TMO])) break; if (_sp > XB_SPIN_CAP) { atomicAdd(&(bar)[XB_TMO], 1u); break; } } } } while (0)
; __device__ __forceinline__ void xcd_barrier(const XcdBarrier& b) {
;     ...
;             XB_SPIN(xb_ld(&bar[XB_XGEN(b.x)]) == gen, bar);
;             __builtin_amdgcn_fence(__ATOMIC_ACQUIRE, "agent");
;             asm volatile("s_waitcnt vmcnt(0)" ::: "memory");
.LBB0_242:
	s_or_b64 exec, exec, s[10:11]
	s_waitcnt vmcnt(0)
	s_waitcnt vmcnt(0)

; __device__ __forceinline__ unsigned xb_ld(unsigned* p)              { return __hip_atomic_load(p, __ATOMIC_RELAXED, __HIP_MEMORY_SCOPE_AGENT); }
; __device__ __forceinline__ unsigned xb_add(unsigned* p, unsigned v) { return __hip_atomic_fetch_add(p, v, __ATOMIC_RELAXED, __HIP_MEMORY_SCOPE_AGENT); }
; #define XB_SPIN(cond, bar) do { unsigned _sp = 0; while (cond) { __builtin_amdgcn_s_sleep(1); \
;     if ((++_sp & 255u) == 0u) { if (xb_ld(&(bar)[XB_TMO])) break; if (_sp > XB_SPIN_CAP) { atomicAdd(&(bar)[XB_TMO], 1u); break; } } } } while (0)
; __device__ __forceinline__ void xcd_barrier(const XcdBarrier& b) {
;     ...
;         const unsigned old = xb_add(&bar[XB_XSUB(b.x)], 1u);
;         const unsigned gen = old / nloc;
;         if (old + 1u == (gen + 1u) * nloc) {
;             __builtin_amdgcn_fence(__ATOMIC_RELEASE, "agent");
;             asm volatile("s_waitcnt vmcnt(0)" ::: "memory");
;             const unsigned og = xb_add(&bar[XB_TOP], 1u);
;             const unsigned tg = og / nx;
;             if (og + 1u == (tg + 1u) * nx) xb_add(&bar[XB_TOPGEN], 1u);
;             else XB_SPIN(xb_ld(&bar[XB_TOPGEN]) == tg, bar);
;             __builtin_amdgcn_fence(__ATOMIC_ACQUIRE, "agent");
;             xb_add(&bar[XB_XGEN(b.x)], 1u);
;             asm volatile("s_waitcnt vmcnt(0)" ::: "memory");
;         } else {
;             XB_SPIN(xb_ld(&bar[XB_XGEN(b.x)]) == gen, bar);
.LBB0_382:
	v_readlane_b32 s0, v247, 55
	v_readlane_b32 s1, v247, 56
	v_cvt_f32_u32_e32 v1, v2
	v_sub_u32_e32 v4, 0, v2
	v_rcp_iflag_f32_e32 v1, v1
	s_nop 1
	buffer_inv sc1
	global_atomic_add v3, v153, v197, s[0:1] sc0
	v_mul_f32_e32 v1, 0x4f7ffffe, v1
	v_cvt_u32_f32_e32 v1, v1
	v_mul_lo_u32 v4, v4, v1
	v_mul_hi_u32 v4, v1, v4
	v_add_u32_e32 v1, v1, v4
	s_waitcnt vmcnt(0)
	v_mul_hi_u32 v1, v3, v1
	v_mul_lo_u32 v4, v1, v2
	v_sub_u32_e32 v4, v3, v4
	v_add_u32_e32 v5, 1, v1
	v_cmp_ge_u32_e32 vcc, v4, v2
	v_add_u32_e32 v3, 1, v3
	s_nop 0
	v_cndmask_b32_e32 v1, v1, v5, vcc
	v_sub_u32_e32 v5, v4, v2
	v_cndmask_b32_e32 v4, v4, v5, vcc
	v_add_u32_e32 v5, 1, v1
	v_cmp_ge_u32_e32 vcc, v4, v2
	s_nop 1
	v_cndmask_b32_e32 v1, v1, v5, vcc
	v_mul_lo_u32 v4, v2, v1
	v_add_u32_e32 v2, v4, v2
	v_cmp_ne_u32_e32 vcc, v3, v2
	s_and_saveexec_b64 s[0:1], vcc
	s_xor_b64 s[0:1], exec, s[0:1]
	s_cbranch_execz .LBB0_396
	v_readlane_b32 s2, v247, 61
	v_readlane_b32 s3, v247, 62
	s_waitcnt lgkmcnt(0)
	s_nop 3
	global_load_dword v0, v153, s[2:3] sc1
	s_waitcnt vmcnt(0)
	v_cmp_eq_u32_e32 vcc, v0, v1
	s_and_saveexec_b64 s[10:11], vcc
	s_cbranch_execz .LBB0_395
	s_mov_b32 s40, 1
	s_mov_b64 s[12:13], 0
	s_branch .LBB0_386

; __device__ __forceinline__ unsigned xb_ld(unsigned* p)              { return __hip_atomic_load(p, __ATOMIC_RELAXED, __HIP_MEMORY_SCOPE_AGENT); }
; __device__ __forceinline__ unsigned xb_add(unsigned* p, unsigned v) { return __hip_atomic_fetch_add(p, v, __ATOMIC_RELAXED, __HIP_MEMORY_SCOPE_AGENT); }
; #define XB_SPIN(cond, bar) do { unsigned _sp = 0; while (cond) { __builtin_amdgcn_s_sleep(1); \
;     if ((++_sp & 255u) == 0u) { if (xb_ld(&(bar)[XB_TMO])) break; if (_sp > XB_SPIN_CAP) { atomicAdd(&(bar)[XB_TMO], 1u); break; } } } } while (0)
; __device__ __forceinline__ void xcd_barrier(const XcdBarrier& b) {
;     ...
;         const unsigned old = xb_add(&bar[XB_XSUB(b.x)], 1u);
;         const unsigned gen = old / nloc;
;         if (old + 1u == (gen + 1u) * nloc) {
;             __builtin_amdgcn_fence(__ATOMIC_RELEASE, "agent");
;             asm volatile("s_waitcnt vmcnt(0)" ::: "memory");
;             const unsigned og = xb_add(&bar[XB_TOP], 1u);
;             const unsigned tg = og / nx;
;             if (og + 1u == (tg + 1u) * nx) xb_add(&bar[XB_TOPGEN], 1u);
;             else XB_SPIN(xb_ld(&bar[XB_TOPGEN]) == tg, bar);
;             __builtin_amdgcn_fence(__ATOMIC_ACQUIRE, "agent");
;             xb_add(&bar[XB_XGEN(b.x)], 1u);
;             asm volatile("s_waitcnt vmcnt(0)" ::: "memory");
;         } else {
;             XB_SPIN(xb_ld(&bar[XB_XGEN(b.x)]) == gen, bar);
.LBB0_790:
	v_readlane_b32 s0, v247, 55
	v_readlane_b32 s1, v247, 56
	v_cvt_f32_u32_e32 v1, v2
	v_sub_u32_e32 v4, 0, v2
	v_rcp_iflag_f32_e32 v1, v1
	s_nop 1
	buffer_inv sc1
	global_atomic_add v3, v153, v197, s[0:1] sc0
	v_mul_f32_e32 v1, 0x4f7ffffe, v1
	v_cvt_u32_f32_e32 v1, v1
	v_mul_lo_u32 v4, v4, v1
	v_mul_hi_u32 v4, v1, v4
	v_add_u32_e32 v1, v1, v4
	s_waitcnt vmcnt(0)
	v_mul_hi_u32 v1, v3, v1
	v_mul_lo_u32 v4, v1, v2
	v_sub_u32_e32 v4, v3, v4
	v_add_u32_e32 v5, 1, v1
	v_cmp_ge_u32_e32 vcc, v4, v2
	v_add_u32_e32 v3, 1, v3
	s_nop 0
	v_cndmask_b32_e32 v1, v1, v5, vcc
	v_sub_u32_e32 v5, v4, v2
	v_cndmask_b32_e32 v4, v4, v5, vcc
	v_add_u32_e32 v5, 1, v1
	v_cmp_ge_u32_e32 vcc, v4, v2
	s_nop 1
	v_cndmask_b32_e32 v1, v1, v5, vcc
	v_mul_lo_u32 v4, v2, v1
	v_add_u32_e32 v2, v4, v2
	v_cmp_ne_u32_e32 vcc, v3, v2
	s_and_saveexec_b64 s[0:1], vcc
	s_xor_b64 s[0:1], exec, s[0:1]
	s_cbranch_execz .LBB0_804
	v_readlane_b32 s2, v247, 61
	v_readlane_b32 s3, v247, 62
	s_waitcnt lgkmcnt(0)
	s_nop 3
	global_load_dword v0, v153, s[2:3] sc1
	s_waitcnt vmcnt(0)
	v_cmp_eq_u32_e32 vcc, v0, v1
	s_and_saveexec_b64 s[10:11], vcc
	s_cbranch_execz .LBB0_803
	s_mov_b32 s5, 1
	s_mov_b64 s[12:13], 0
	s_branch .LBB0_794

; __device__ __forceinline__ unsigned xb_ld(unsigned* p)              { return __hip_atomic_load(p, __ATOMIC_RELAXED, __HIP_MEMORY_SCOPE_AGENT); }
; __device__ __forceinline__ unsigned xb_add(unsigned* p, unsigned v) { return __hip_atomic_fetch_add(p, v, __ATOMIC_RELAXED, __HIP_MEMORY_SCOPE_AGENT); }
; #define XB_SPIN(cond, bar) do { unsigned _sp = 0; while (cond) { __builtin_amdgcn_s_sleep(1); \
;     if ((++_sp & 255u) == 0u) { if (xb_ld(&(bar)[XB_TMO])) break; if (_sp > XB_SPIN_CAP) { atomicAdd(&(bar)[XB_TMO], 1u); break; } } } } while (0)
; __device__ __forceinline__ void xcd_barrier(const XcdBarrier& b) {
;     ...
;         const unsigned old = xb_add(&bar[XB_XSUB(b.x)], 1u);
;         const unsigned gen = old / nloc;
;         if (old + 1u == (gen + 1u) * nloc) {
;             __builtin_amdgcn_fence(__ATOMIC_RELEASE, "agent");
;             asm volatile("s_waitcnt vmcnt(0)" ::: "memory");
;             const unsigned og = xb_add(&bar[XB_TOP], 1u);
;             const unsigned tg = og / nx;
;             if (og + 1u == (tg + 1u) * nx) xb_add(&bar[XB_TOPGEN], 1u);
;             else XB_SPIN(xb_ld(&bar[XB_TOPGEN]) == tg, bar);
;             __builtin_amdgcn_fence(__ATOMIC_ACQUIRE, "agent");
;             xb_add(&bar[XB_XGEN(b.x)], 1u);
;             asm volatile("s_waitcnt vmcnt(0)" ::: "memory");
;         } else {
;             XB_SPIN(xb_ld(&bar[XB_XGEN(b.x)]) == gen, bar);
.LBB0_1110:
	v_readlane_b32 s0, v247, 55
	v_readlane_b32 s1, v247, 56
	v_cvt_f32_u32_e32 v1, v2
	v_sub_u32_e32 v4, 0, v2
	v_rcp_iflag_f32_e32 v1, v1
	s_nop 1
	buffer_inv sc1
	global_atomic_add v3, v153, v197, s[0:1] sc0
	v_mul_f32_e32 v1, 0x4f7ffffe, v1
	v_cvt_u32_f32_e32 v1, v1
	v_mul_lo_u32 v4, v4, v1
	v_mul_hi_u32 v4, v1, v4
	v_add_u32_e32 v1, v1, v4
	s_waitcnt vmcnt(0)
	v_mul_hi_u32 v1, v3, v1
	v_mul_lo_u32 v4, v1, v2
	v_sub_u32_e32 v4, v3, v4
	v_add_u32_e32 v5, 1, v1
	v_cmp_ge_u32_e32 vcc, v4, v2
	v_add_u32_e32 v3, 1, v3
	s_nop 0
	v_cndmask_b32_e32 v1, v1, v5, vcc
	v_sub_u32_e32 v5, v4, v2
	v_cndmask_b32_e32 v4, v4, v5, vcc
	v_add_u32_e32 v5, 1, v1
	v_cmp_ge_u32_e32 vcc, v4, v2
	s_nop 1
	v_cndmask_b32_e32 v1, v1, v5, vcc
	v_mul_lo_u32 v4, v2, v1
	v_add_u32_e32 v2, v4, v2
	v_cmp_ne_u32_e32 vcc, v3, v2
	s_and_saveexec_b64 s[0:1], vcc
	s_xor_b64 s[0:1], exec, s[0:1]
	s_cbranch_execz .LBB0_1124
	v_readlane_b32 s2, v247, 61
	v_readlane_b32 s3, v247, 62
	s_waitcnt lgkmcnt(0)
	s_nop 3
	global_load_dword v0, v153, s[2:3] sc1
	s_waitcnt vmcnt(0)
	v_cmp_eq_u32_e32 vcc, v0, v1
	s_and_saveexec_b64 s[8:9], vcc
	s_cbranch_execz .LBB0_1123
	s_mov_b32 s41, 1
	s_mov_b64 s[10:11], 0
	s_branch .LBB0_1114

; __device__ __forceinline__ unsigned xb_ld(unsigned* p)              { return __hip_atomic_load(p, __ATOMIC_RELAXED, __HIP_MEMORY_SCOPE_AGENT); }
; #define XB_SPIN(cond, bar) do { unsigned _sp = 0; while (cond) { __builtin_amdgcn_s_sleep(1); \
;     if ((++_sp & 255u) == 0u) { if (xb_ld(&(bar)[XB_TMO])) break; if (_sp > XB_SPIN_CAP) { atomicAdd(&(bar)[XB_TMO], 1u); break; } } } } while (0)
; __device__ __forceinline__ void xcd_barrier(const XcdBarrier& b) {
;     ...
;             XB_SPIN(xb_ld(&bar[XB_XGEN(b.x)]) == gen, bar);
;             __builtin_amdgcn_fence(__ATOMIC_ACQUIRE, "agent");
;             asm volatile("s_waitcnt vmcnt(0)" ::: "memory");
.LBB0_1123:
	s_or_b64 exec, exec, s[8:9]
	s_waitcnt vmcnt(0)
	s_waitcnt vmcnt(0)

; __device__ __forceinline__ unsigned xb_ld(unsigned* p)              { return __hip_atomic_load(p, __ATOMIC_RELAXED, __HIP_MEMORY_SCOPE_AGENT); }
; __device__ __forceinline__ unsigned xb_add(unsigned* p, unsigned v) { return __hip_atomic_fetch_add(p, v, __ATOMIC_RELAXED, __HIP_MEMORY_SCOPE_AGENT); }
; #define XB_SPIN(cond, bar) do { unsigned _sp = 0; while (cond) { __builtin_amdgcn_s_sleep(1); \
;     if ((++_sp & 255u) == 0u) { if (xb_ld(&(bar)[XB_TMO])) break; if (_sp > XB_SPIN_CAP) { atomicAdd(&(bar)[XB_TMO], 1u); break; } } } } while (0)
; __device__ __forceinline__ void xcd_barrier(const XcdBarrier& b) {
;     ...
;         const unsigned old = xb_add(&bar[XB_XSUB(b.x)], 1u);
;         const unsigned gen = old / nloc;
;         if (old + 1u == (gen + 1u) * nloc) {
;             __builtin_amdgcn_fence(__ATOMIC_RELEASE, "agent");
;             asm volatile("s_waitcnt vmcnt(0)" ::: "memory");
;             const unsigned og = xb_add(&bar[XB_TOP], 1u);
;             const unsigned tg = og / nx;
;             if (og + 1u == (tg + 1u) * nx) xb_add(&bar[XB_TOPGEN], 1u);
;             else XB_SPIN(xb_ld(&bar[XB_TOPGEN]) == tg, bar);
;             __builtin_amdgcn_fence(__ATOMIC_ACQUIRE, "agent");
;             xb_add(&bar[XB_XGEN(b.x)], 1u);
;             asm volatile("s_waitcnt vmcnt(0)" ::: "memory");
;         } else {
;             XB_SPIN(xb_ld(&bar[XB_XGEN(b.x)]) == gen, bar);
.LBB0_1328:
	v_readlane_b32 s0, v247, 55
	v_readlane_b32 s1, v247, 56
	v_cvt_f32_u32_e32 v1, v2
	v_sub_u32_e32 v4, 0, v2
	v_rcp_iflag_f32_e32 v1, v1
	s_nop 1
	buffer_inv sc1
	global_atomic_add v3, v153, v197, s[0:1] sc0
	v_mul_f32_e32 v1, 0x4f7ffffe, v1
	v_cvt_u32_f32_e32 v1, v1
	v_mul_lo_u32 v4, v4, v1
	v_mul_hi_u32 v4, v1, v4
	v_add_u32_e32 v1, v1, v4
	s_waitcnt vmcnt(0)
	v_mul_hi_u32 v1, v3, v1
	v_mul_lo_u32 v4, v1, v2
	v_sub_u32_e32 v4, v3, v4
	v_add_u32_e32 v5, 1, v1
	v_cmp_ge_u32_e32 vcc, v4, v2
	v_add_u32_e32 v3, 1, v3
	s_nop 0
	v_cndmask_b32_e32 v1, v1, v5, vcc
	v_sub_u32_e32 v5, v4, v2
	v_cndmask_b32_e32 v4, v4, v5, vcc
	v_add_u32_e32 v5, 1, v1
	v_cmp_ge_u32_e32 vcc, v4, v2
	s_nop 1
	v_cndmask_b32_e32 v1, v1, v5, vcc
	v_mul_lo_u32 v4, v2, v1
	v_add_u32_e32 v2, v4, v2
	v_cmp_ne_u32_e32 vcc, v3, v2
	s_and_saveexec_b64 s[0:1], vcc
	s_xor_b64 s[0:1], exec, s[0:1]
	s_cbranch_execz .LBB0_1342
	v_readlane_b32 s2, v247, 61
	v_readlane_b32 s3, v247, 62
	s_waitcnt lgkmcnt(0)
	s_nop 3
	global_load_dword v0, v153, s[2:3] sc1
	s_waitcnt vmcnt(0)
	v_cmp_eq_u32_e32 vcc, v0, v1
	s_and_saveexec_b64 s[10:11], vcc
	s_cbranch_execz .LBB0_1341
	s_mov_b32 s43, 1
	s_mov_b64 s[12:13], 0
	s_branch .LBB0_1332

; __device__ __forceinline__ unsigned xb_ld(unsigned* p)              { return __hip_atomic_load(p, __ATOMIC_RELAXED, __HIP_MEMORY_SCOPE_AGENT); }
; __device__ __forceinline__ unsigned xb_add(unsigned* p, unsigned v) { return __hip_atomic_fetch_add(p, v, __ATOMIC_RELAXED, __HIP_MEMORY_SCOPE_AGENT); }
; #define XB_SPIN(cond, bar) do { unsigned _sp = 0; while (cond) { __builtin_amdgcn_s_sleep(1); \
;     if ((++_sp & 255u) == 0u) { if (xb_ld(&(bar)[XB_TMO])) break; if (_sp > XB_SPIN_CAP) { atomicAdd(&(bar)[XB_TMO], 1u); break; } } } } while (0)
; __device__ __forceinline__ void xcd_barrier(const XcdBarrier& b) {
;     ...
;         const unsigned old = xb_add(&bar[XB_XSUB(b.x)], 1u);
;         const unsigned gen = old / nloc;
;         if (old + 1u == (gen + 1u) * nloc) {
;             __builtin_amdgcn_fence(__ATOMIC_RELEASE, "agent");
;             asm volatile("s_waitcnt vmcnt(0)" ::: "memory");
;             const unsigned og = xb_add(&bar[XB_TOP], 1u);
;             const unsigned tg = og / nx;
;             if (og + 1u == (tg + 1u) * nx) xb_add(&bar[XB_TOPGEN], 1u);
;             else XB_SPIN(xb_ld(&bar[XB_TOPGEN]) == tg, bar);
;             __builtin_amdgcn_fence(__ATOMIC_ACQUIRE, "agent");
;             xb_add(&bar[XB_XGEN(b.x)], 1u);
;             asm volatile("s_waitcnt vmcnt(0)" ::: "memory");
;         } else {
;             XB_SPIN(xb_ld(&bar[XB_XGEN(b.x)]) == gen, bar);
.LBB0_1707:
	v_readlane_b32 s0, v247, 55
	v_readlane_b32 s1, v247, 56
	v_cvt_f32_u32_e32 v1, v2
	v_sub_u32_e32 v4, 0, v2
	v_rcp_iflag_f32_e32 v1, v1
	s_nop 1
	buffer_inv sc1
	global_atomic_add v3, v153, v197, s[0:1] sc0
	v_mul_f32_e32 v1, 0x4f7ffffe, v1
	v_cvt_u32_f32_e32 v1, v1
	v_mul_lo_u32 v4, v4, v1
	v_mul_hi_u32 v4, v1, v4
	v_add_u32_e32 v1, v1, v4
	s_waitcnt vmcnt(0)
	v_mul_hi_u32 v1, v3, v1
	v_mul_lo_u32 v4, v1, v2
	v_sub_u32_e32 v4, v3, v4
	v_add_u32_e32 v5, 1, v1
	v_cmp_ge_u32_e32 vcc, v4, v2
	v_add_u32_e32 v3, 1, v3
	s_nop 0
	v_cndmask_b32_e32 v1, v1, v5, vcc
	v_sub_u32_e32 v5, v4, v2
	v_cndmask_b32_e32 v4, v4, v5, vcc
	v_add_u32_e32 v5, 1, v1
	v_cmp_ge_u32_e32 vcc, v4, v2
	s_nop 1
	v_cndmask_b32_e32 v1, v1, v5, vcc
	v_mul_lo_u32 v4, v2, v1
	v_add_u32_e32 v2, v4, v2
	v_cmp_ne_u32_e32 vcc, v3, v2
	s_and_saveexec_b64 s[0:1], vcc
	s_xor_b64 s[0:1], exec, s[0:1]
	s_cbranch_execz .LBB0_1721
	v_readlane_b32 s2, v247, 61
	v_readlane_b32 s3, v247, 62
	s_waitcnt lgkmcnt(0)
	s_nop 3
	global_load_dword v0, v153, s[2:3] sc1
	s_waitcnt vmcnt(0)
	v_cmp_eq_u32_e32 vcc, v0, v1
	s_and_saveexec_b64 s[8:9], vcc
	s_cbranch_execz .LBB0_1720
	s_mov_b32 s5, 1
	s_mov_b64 s[10:11], 0
	s_branch .LBB0_1711
